# grid barrier: XCD leader leaves without waiting for the ack of its own generation add (on top of v33)
# baseline (speedup 1.0000x reference)
.LBB0_321:
	s_or_b64 exec, exec, s[30:31]
.LBB0_322:
	s_or_b64 exec, exec, s[0:1]
	s_waitcnt lgkmcnt(0)
	s_barrier

.LBB0_538:
	s_or_b64 exec, exec, s[30:31]
.LBB0_539:
	s_or_b64 exec, exec, s[0:1]
	s_waitcnt lgkmcnt(0)
	s_barrier

.LBB0_687:
	s_or_b64 exec, exec, s[30:31]
.LBB0_688:
	s_or_b64 exec, exec, s[0:1]
	s_waitcnt lgkmcnt(0)
	s_barrier

.LBB0_1067:
	s_or_b64 exec, exec, s[30:31]
.LBB0_1068:
	s_or_b64 exec, exec, s[0:1]
	s_waitcnt lgkmcnt(0)
	s_barrier

.LBB0_1176:
	s_or_b64 exec, exec, s[30:31]
.LBB0_1177:
	s_or_b64 exec, exec, s[0:1]
	s_waitcnt lgkmcnt(0)
	s_barrier

.LBB0_1236:
	s_or_b64 exec, exec, s[30:31]
.LBB0_1237:
	s_or_b64 exec, exec, s[0:1]
	s_waitcnt lgkmcnt(0)
	s_barrier

.LBB0_1389:
	s_or_b64 exec, exec, s[30:31]
.LBB0_1390:
	s_or_b64 exec, exec, s[0:1]
	s_waitcnt lgkmcnt(0)
	s_barrier

.LBB0_1454:
	s_or_b64 exec, exec, s[30:31]
.LBB0_1455:
	s_or_b64 exec, exec, s[0:1]
	s_waitcnt lgkmcnt(0)
	s_barrier

.LBB0_1612:
	s_or_b64 exec, exec, s[30:31]
.LBB0_1613:
	s_or_b64 exec, exec, s[0:1]
	s_waitcnt lgkmcnt(0)
	s_barrier

.LBB0_1822:
	s_or_b64 exec, exec, s[30:31]
.LBB0_1823:
	s_or_b64 exec, exec, s[0:1]
	s_waitcnt lgkmcnt(0)
	s_barrier

.LBB0_1966:
	s_or_b64 exec, exec, s[30:31]
.LBB0_1967:
	s_or_b64 exec, exec, s[0:1]
	s_waitcnt lgkmcnt(0)
	s_barrier
	s_getpc_b64 s[98:99]
